# P8 out-projection epilogue: residual rows x prefetched 3 row-iterations ahead into free VGPRs (one counted wait per iteration) on top of the batched w_router prologue
# baseline (speedup 1.0000x reference)
.LBB0_740:
	v_mov_b32_e32 v132, v0
	s_lshl_b32 s31, s40, 8
	v_readfirstlane_b32 s4, v132
	s_and_b32 s5, s4, 0xc0
	s_ashr_i32 s4, s4, 2
	s_andn2_b32 s4, s4, 63
	s_add_i32 s4, s4, s31
	s_lshl_b32 s31, s58, 8
	s_or_b32 s5, s5, s31
	v_and_or_b32 v162, v132, 15, s4
	v_and_or_b32 v160, v132, 48, s5
	v_ashrrev_i32_e32 v163, 31, v162
	v_ashrrev_i32_e32 v161, 31, v160
	v_lshlrev_b64 v[132:133], 11, v[162:163]
	v_lshl_add_u64 v[158:159], v[132:133], 0, v[160:161]
	v_lshl_add_u64 v[130:131], v[160:161], 2, s[14:15]
	v_lshl_add_u64 v[182:183], v[158:159], 2, s[10:11]
	v_mov_b32_e32 v240, 0x20000
	v_mov_b32_e32 v241, 0
	v_mov_b32_e32 v244, 0x100000
	v_mov_b32_e32 v245, 0
	v_lshl_add_u64 v[242:243], v[182:183], 0, v[240:241]
	v_lshl_add_u64 v[244:245], v[182:183], 0, v[244:245]
	v_lshl_add_u64 v[246:247], v[244:245], 0, v[240:241]
	v_lshl_add_u64 v[248:249], v[246:247], 0, v[240:241]
	v_lshl_add_u64 v[250:251], v[248:249], 0, v[240:241]
	global_load_dwordx4 v[170:173], v[182:183], off
	global_load_dwordx4 v[142:145], v[130:131], off
	global_load_dwordx4 v[134:137], v[130:131], off offset:16
	global_load_dwordx4 v[174:177], v[182:183], off offset:16
	global_load_dwordx4 v[178:181], v[182:183], off offset:32
	global_load_dwordx4 v[138:141], v[130:131], off offset:32
	s_nop 0
	global_load_dwordx4 v[130:133], v[130:131], off offset:48
	s_nop 0
	global_load_dwordx4 v[182:185], v[182:183], off offset:48
	global_load_dwordx4 v[192:195], v[242:243], off
	global_load_dwordx4 v[196:199], v[242:243], off offset:16
	global_load_dwordx4 v[200:203], v[242:243], off offset:32
	global_load_dwordx4 v[204:207], v[242:243], off offset:48
	v_lshl_add_u64 v[242:243], v[242:243], 0, v[240:241]
	global_load_dwordx4 v[208:211], v[242:243], off
	global_load_dwordx4 v[212:215], v[242:243], off offset:16
	global_load_dwordx4 v[216:219], v[242:243], off offset:32
	global_load_dwordx4 v[220:223], v[242:243], off offset:48
	v_lshl_add_u64 v[242:243], v[242:243], 0, v[240:241]
	global_load_dwordx4 v[224:227], v[242:243], off
	global_load_dwordx4 v[228:231], v[242:243], off offset:16
	global_load_dwordx4 v[232:235], v[242:243], off offset:32
	global_load_dwordx4 v[236:239], v[242:243], off offset:48
	v_or_b32_e32 v186, 16, v162
	v_ashrrev_i32_e32 v187, 31, v186
	v_lshlrev_b64 v[186:187], 11, v[186:187]
	v_lshl_add_u64 v[188:189], v[158:159], 1, s[16:17]
	v_lshl_add_u64 v[186:187], v[186:187], 0, v[160:161]
	v_lshl_add_u64 v[190:191], v[186:187], 2, s[10:11]
	s_andn2_b64 vcc, exec, s[6:7]
	s_mov_b64 s[4:5], -1
	s_waitcnt vmcnt(12)
	v_pk_fma_f32 v[128:129], v[128:129], v[144:145], v[172:173]
	v_pk_fma_f32 v[126:127], v[126:127], v[142:143], v[170:171]
	v_pk_fma_f32 v[124:125], v[124:125], v[136:137], v[176:177]
	v_pk_fma_f32 v[122:123], v[122:123], v[134:135], v[174:175]
	v_pk_fma_f32 v[120:121], v[120:121], v[140:141], v[180:181]
	v_pk_fma_f32 v[118:119], v[118:119], v[138:139], v[178:179]
	v_pk_fma_f32 v[170:171], v[116:117], v[132:133], v[184:185]
	v_pk_fma_f32 v[172:173], v[114:115], v[130:131], v[182:183]
	v_cvt_pk_bf16_f32 v114, v126, v127
	v_cvt_pk_bf16_f32 v115, v128, v129
	v_cvt_pk_bf16_f32 v116, v122, v123
	v_cvt_pk_bf16_f32 v117, v124, v125
	v_cvt_pk_bf16_f32 v118, v118, v119
	v_cvt_pk_bf16_f32 v119, v120, v121
	s_nop 0
	v_cvt_pk_bf16_f32 v120, v172, v173
	v_cvt_pk_bf16_f32 v121, v170, v171
	global_store_dwordx4 v[188:189], v[114:117], off
	global_store_dwordx4 v[188:189], v[118:121], off offset:16
	s_nop 0
	v_or_b32_e32 v170, 32, v162
	v_ashrrev_i32_e32 v171, 31, v170
	v_lshlrev_b64 v[170:171], 11, v[170:171]
	v_lshl_add_u64 v[170:171], v[170:171], 0, v[160:161]
	v_lshl_add_u64 v[172:173], v[186:187], 1, s[16:17]
	v_lshl_add_u64 v[174:175], v[170:171], 2, s[10:11]
	s_waitcnt vmcnt(10)
	v_pk_fma_f32 v[112:113], v[112:113], v[144:145], v[194:195]
	v_pk_fma_f32 v[110:111], v[110:111], v[142:143], v[192:193]
	v_pk_fma_f32 v[108:109], v[108:109], v[136:137], v[198:199]
	v_pk_fma_f32 v[106:107], v[106:107], v[134:135], v[196:197]
	v_pk_fma_f32 v[104:105], v[104:105], v[140:141], v[202:203]
	v_pk_fma_f32 v[102:103], v[102:103], v[138:139], v[200:201]
	v_pk_fma_f32 v[192:193], v[100:101], v[132:133], v[206:207]
	v_pk_fma_f32 v[194:195], v[98:99], v[130:131], v[204:205]
	v_cvt_pk_bf16_f32 v98, v110, v111
	v_cvt_pk_bf16_f32 v99, v112, v113
	v_cvt_pk_bf16_f32 v100, v106, v107
	v_cvt_pk_bf16_f32 v101, v108, v109
	v_cvt_pk_bf16_f32 v102, v102, v103
	v_cvt_pk_bf16_f32 v103, v104, v105
	s_nop 0
	v_cvt_pk_bf16_f32 v104, v194, v195
	v_cvt_pk_bf16_f32 v105, v192, v193
	global_store_dwordx4 v[172:173], v[98:101], off
	global_store_dwordx4 v[172:173], v[102:105], off offset:16
	s_nop 0
	global_load_dwordx4 v[192:195], v[244:245], off
	global_load_dwordx4 v[196:199], v[244:245], off offset:16
	global_load_dwordx4 v[200:203], v[244:245], off offset:32
	global_load_dwordx4 v[204:207], v[244:245], off offset:48
	v_or_b32_e32 v114, 48, v162
	v_ashrrev_i32_e32 v115, 31, v114
	v_lshlrev_b64 v[114:115], 11, v[114:115]
	v_lshl_add_u64 v[114:115], v[114:115], 0, v[160:161]
	v_lshl_add_u64 v[116:117], v[170:171], 1, s[16:17]
	v_lshl_add_u64 v[118:119], v[114:115], 2, s[10:11]
	s_waitcnt vmcnt(12)
	v_pk_fma_f32 v[96:97], v[96:97], v[144:145], v[210:211]
	v_pk_fma_f32 v[94:95], v[94:95], v[142:143], v[208:209]
	v_pk_fma_f32 v[92:93], v[92:93], v[136:137], v[214:215]
	v_pk_fma_f32 v[90:91], v[90:91], v[134:135], v[212:213]
	v_pk_fma_f32 v[88:89], v[88:89], v[140:141], v[218:219]
	v_pk_fma_f32 v[86:87], v[86:87], v[138:139], v[216:217]
	v_pk_fma_f32 v[208:209], v[84:85], v[132:133], v[222:223]
	v_pk_fma_f32 v[210:211], v[82:83], v[130:131], v[220:221]
	v_cvt_pk_bf16_f32 v82, v94, v95
	v_cvt_pk_bf16_f32 v83, v96, v97
	v_cvt_pk_bf16_f32 v84, v90, v91
	v_cvt_pk_bf16_f32 v85, v92, v93
	v_cvt_pk_bf16_f32 v86, v86, v87
	v_cvt_pk_bf16_f32 v87, v88, v89
	s_nop 0
	v_cvt_pk_bf16_f32 v88, v210, v211
	v_cvt_pk_bf16_f32 v89, v208, v209
	global_store_dwordx4 v[116:117], v[82:85], off
	global_store_dwordx4 v[116:117], v[86:89], off offset:16
	s_nop 0
	global_load_dwordx4 v[208:211], v[246:247], off
	global_load_dwordx4 v[212:215], v[246:247], off offset:16
	global_load_dwordx4 v[216:219], v[246:247], off offset:32
	global_load_dwordx4 v[220:223], v[246:247], off offset:48
	v_lshl_add_u64 v[98:99], v[158:159], 0, s[22:23]
	v_lshl_add_u64 v[100:101], v[114:115], 1, s[16:17]
	v_lshl_add_u64 v[102:103], v[98:99], 2, s[10:11]
	s_waitcnt vmcnt(14)
	v_pk_fma_f32 v[80:81], v[80:81], v[144:145], v[226:227]
	v_pk_fma_f32 v[78:79], v[78:79], v[142:143], v[224:225]
	v_pk_fma_f32 v[76:77], v[76:77], v[136:137], v[230:231]
	v_pk_fma_f32 v[74:75], v[74:75], v[134:135], v[228:229]
	v_pk_fma_f32 v[72:73], v[72:73], v[140:141], v[234:235]
	v_pk_fma_f32 v[70:71], v[70:71], v[138:139], v[232:233]
	v_pk_fma_f32 v[224:225], v[68:69], v[132:133], v[238:239]
	v_pk_fma_f32 v[226:227], v[66:67], v[130:131], v[236:237]
	v_cvt_pk_bf16_f32 v66, v78, v79
	v_cvt_pk_bf16_f32 v67, v80, v81
	v_cvt_pk_bf16_f32 v68, v74, v75
	v_cvt_pk_bf16_f32 v69, v76, v77
	v_cvt_pk_bf16_f32 v70, v70, v71
	v_cvt_pk_bf16_f32 v71, v72, v73
	s_nop 0
	v_cvt_pk_bf16_f32 v72, v226, v227
	v_cvt_pk_bf16_f32 v73, v224, v225
	global_store_dwordx4 v[100:101], v[66:69], off
	global_store_dwordx4 v[100:101], v[70:73], off offset:16
	s_nop 0
	global_load_dwordx4 v[224:227], v[248:249], off
	global_load_dwordx4 v[228:231], v[248:249], off offset:16
	global_load_dwordx4 v[232:235], v[248:249], off offset:32
	global_load_dwordx4 v[236:239], v[248:249], off offset:48
	v_lshl_add_u64 v[82:83], v[158:159], 0, s[24:25]
	v_lshl_add_u64 v[84:85], v[98:99], 1, s[16:17]
	v_lshl_add_u64 v[86:87], v[82:83], 2, s[10:11]
	s_waitcnt vmcnt(12)
	v_pk_fma_f32 v[64:65], v[64:65], v[144:145], v[194:195]
	v_pk_fma_f32 v[62:63], v[62:63], v[142:143], v[192:193]
	v_pk_fma_f32 v[60:61], v[60:61], v[136:137], v[198:199]
	v_pk_fma_f32 v[58:59], v[58:59], v[134:135], v[196:197]
	v_pk_fma_f32 v[56:57], v[56:57], v[140:141], v[202:203]
	v_pk_fma_f32 v[54:55], v[54:55], v[138:139], v[200:201]
	v_pk_fma_f32 v[192:193], v[52:53], v[132:133], v[206:207]
	v_pk_fma_f32 v[194:195], v[50:51], v[130:131], v[204:205]
	v_cvt_pk_bf16_f32 v50, v62, v63
	v_cvt_pk_bf16_f32 v51, v64, v65
	v_cvt_pk_bf16_f32 v52, v58, v59
	v_cvt_pk_bf16_f32 v53, v60, v61
	v_cvt_pk_bf16_f32 v54, v54, v55
	v_cvt_pk_bf16_f32 v55, v56, v57
	s_nop 0
	v_cvt_pk_bf16_f32 v56, v194, v195
	v_cvt_pk_bf16_f32 v57, v192, v193
	global_store_dwordx4 v[84:85], v[50:53], off
	global_store_dwordx4 v[84:85], v[54:57], off offset:16
	s_nop 0
	global_load_dwordx4 v[192:195], v[250:251], off
	global_load_dwordx4 v[196:199], v[250:251], off offset:16
	global_load_dwordx4 v[200:203], v[250:251], off offset:32
	global_load_dwordx4 v[204:207], v[250:251], off offset:48
	v_lshl_add_u64 v[66:67], v[158:159], 0, s[26:27]
	v_lshl_add_u64 v[68:69], v[82:83], 1, s[16:17]
	v_lshl_add_u64 v[70:71], v[66:67], 2, s[10:11]
	s_waitcnt vmcnt(12)
	v_pk_fma_f32 v[48:49], v[48:49], v[144:145], v[210:211]
	v_pk_fma_f32 v[46:47], v[46:47], v[142:143], v[208:209]
	v_pk_fma_f32 v[44:45], v[44:45], v[136:137], v[214:215]
	v_pk_fma_f32 v[42:43], v[42:43], v[134:135], v[212:213]
	v_pk_fma_f32 v[40:41], v[40:41], v[140:141], v[218:219]
	v_pk_fma_f32 v[38:39], v[38:39], v[138:139], v[216:217]
	v_pk_fma_f32 v[208:209], v[36:37], v[132:133], v[222:223]
	v_pk_fma_f32 v[210:211], v[34:35], v[130:131], v[220:221]
	v_cvt_pk_bf16_f32 v34, v46, v47
	v_cvt_pk_bf16_f32 v35, v48, v49
	v_cvt_pk_bf16_f32 v36, v42, v43
	v_cvt_pk_bf16_f32 v37, v44, v45
	v_cvt_pk_bf16_f32 v38, v38, v39
	v_cvt_pk_bf16_f32 v39, v40, v41
	s_nop 0
	v_cvt_pk_bf16_f32 v40, v210, v211
	v_cvt_pk_bf16_f32 v41, v208, v209
	global_store_dwordx4 v[68:69], v[34:37], off
	global_store_dwordx4 v[68:69], v[38:41], off offset:16
	s_nop 0
	v_lshl_add_u64 v[50:51], v[158:159], 0, s[28:29]
	v_lshl_add_u64 v[52:53], v[66:67], 1, s[16:17]
	v_lshl_add_u64 v[54:55], v[50:51], 2, s[10:11]
	s_waitcnt vmcnt(8)
	v_pk_fma_f32 v[32:33], v[32:33], v[144:145], v[226:227]
	v_pk_fma_f32 v[30:31], v[30:31], v[142:143], v[224:225]
	v_pk_fma_f32 v[28:29], v[28:29], v[136:137], v[230:231]
	v_pk_fma_f32 v[26:27], v[26:27], v[134:135], v[228:229]
	v_pk_fma_f32 v[24:25], v[24:25], v[140:141], v[234:235]
	v_pk_fma_f32 v[22:23], v[22:23], v[138:139], v[232:233]
	v_pk_fma_f32 v[224:225], v[20:21], v[132:133], v[238:239]
	v_pk_fma_f32 v[226:227], v[18:19], v[130:131], v[236:237]
	v_cvt_pk_bf16_f32 v18, v30, v31
	v_cvt_pk_bf16_f32 v19, v32, v33
	v_cvt_pk_bf16_f32 v20, v26, v27
	v_cvt_pk_bf16_f32 v21, v28, v29
	v_cvt_pk_bf16_f32 v22, v22, v23
	v_cvt_pk_bf16_f32 v23, v24, v25
	s_nop 0
	v_cvt_pk_bf16_f32 v24, v226, v227
	v_cvt_pk_bf16_f32 v25, v224, v225
	global_store_dwordx4 v[52:53], v[18:21], off
	global_store_dwordx4 v[52:53], v[22:25], off offset:16
	s_nop 0
	v_lshl_add_u64 v[34:35], v[50:51], 1, s[16:17]
	s_waitcnt vmcnt(4)
	v_pk_fma_f32 v[16:17], v[16:17], v[144:145], v[194:195]
	v_pk_fma_f32 v[14:15], v[14:15], v[142:143], v[192:193]
	v_pk_fma_f32 v[12:13], v[12:13], v[136:137], v[198:199]
	v_pk_fma_f32 v[10:11], v[10:11], v[134:135], v[196:197]
	v_pk_fma_f32 v[8:9], v[8:9], v[140:141], v[202:203]
	v_pk_fma_f32 v[6:7], v[6:7], v[138:139], v[200:201]
	v_pk_fma_f32 v[192:193], v[4:5], v[132:133], v[206:207]
	v_pk_fma_f32 v[194:195], v[2:3], v[130:131], v[204:205]
	v_cvt_pk_bf16_f32 v2, v14, v15
	v_cvt_pk_bf16_f32 v3, v16, v17
	v_cvt_pk_bf16_f32 v4, v10, v11
	v_cvt_pk_bf16_f32 v5, v12, v13
	v_cvt_pk_bf16_f32 v6, v6, v7
	v_cvt_pk_bf16_f32 v7, v8, v9
	s_nop 0
	v_cvt_pk_bf16_f32 v8, v194, v195
	v_cvt_pk_bf16_f32 v9, v192, v193
	global_store_dwordx4 v[34:35], v[2:5], off
	global_store_dwordx4 v[34:35], v[6:9], off offset:16
	s_cbranch_vccnz .LBB0_729
	s_andn2_b64 vcc, exec, s[12:13]
	s_cbranch_vccnz .LBB0_728
	s_barrier
	s_branch .LBB0_728
